# fp8 GEMM stage bodies: first fragment-read burst ordered by first use with counted lgkmcnt waits per MFMA (pipe starts after 4 reads instead of 12), all nine bodies
# baseline (speedup 1.0000x reference)
.LBB0_248:
	s_cmp_lg_u32 s26, 0
	s_cbranch_scc1 .Lp1b_XT
	s_and_b32 s5, s4, 0x10000
	v_or_b32_e32 v2, s5, v250
	v_xor_b32_e32 v6, 64, v2
	v_add_u32_e32 v68, s5, v249
	v_xor_b32_e32 v66, 64, v68
	ds_read_b128 v[58:61], v68 offset:0
	ds_read_b128 v[62:65], v66 offset:0
	ds_read_b128 v[26:29], v2 offset:0
	ds_read_b128 v[30:33], v6 offset:0
	ds_read_b128 v[18:21], v2 offset:2048
	ds_read_b128 v[22:25], v6 offset:2048
	ds_read_b128 v[10:13], v2 offset:4096
	ds_read_b128 v[14:17], v6 offset:4096
	ds_read_b128 v[2:5], v2 offset:6144
	ds_read_b128 v[6:9], v6 offset:6144
	ds_read_b128 v[42:45], v68 offset:2048
	ds_read_b128 v[46:49], v66 offset:2048
	ds_read_b128 v[50:53], v68 offset:4096
	ds_read_b128 v[54:57], v66 offset:4096
	ds_read_b128 v[34:37], v68 offset:6144
	ds_read_b128 v[38:41], v66 offset:6144
	s_nop 0
	s_waitcnt lgkmcnt(12)
	v_mfma_scale_f32_16x16x128_f8f6f4 v[194:197], v[58:65], v[26:33], v[194:197], v218, v218 op_sel_hi:[0,0,0]
	s_waitcnt lgkmcnt(10)
	v_mfma_scale_f32_16x16x128_f8f6f4 v[190:193], v[58:65], v[18:25], v[190:193], v218, v218 op_sel_hi:[0,0,0]
	s_waitcnt lgkmcnt(8)
	v_mfma_scale_f32_16x16x128_f8f6f4 v[186:189], v[58:65], v[10:17], v[186:189], v218, v218 op_sel_hi:[0,0,0]
	s_waitcnt lgkmcnt(6)
	v_mfma_scale_f32_16x16x128_f8f6f4 v[182:185], v[58:65], v[2:9], v[182:185], v218, v218 op_sel_hi:[0,0,0]
	s_waitcnt lgkmcnt(4)
	v_mfma_scale_f32_16x16x128_f8f6f4 v[178:181], v[42:49], v[26:33], v[178:181], v218, v218 op_sel_hi:[0,0,0]
	v_mfma_scale_f32_16x16x128_f8f6f4 v[174:177], v[42:49], v[18:25], v[174:177], v218, v218 op_sel_hi:[0,0,0]
	v_mfma_scale_f32_16x16x128_f8f6f4 v[170:173], v[42:49], v[10:17], v[170:173], v218, v218 op_sel_hi:[0,0,0]
	v_mfma_scale_f32_16x16x128_f8f6f4 v[166:169], v[42:49], v[2:9], v[166:169], v218, v218 op_sel_hi:[0,0,0]
	ds_read_b128 v[58:61], v68 offset:8192
	ds_read_b128 v[62:65], v66 offset:8192
	ds_read_b128 v[42:45], v68 offset:10240
	ds_read_b128 v[46:49], v66 offset:10240
	s_waitcnt lgkmcnt(4)
	v_mfma_scale_f32_16x16x128_f8f6f4 v[162:165], v[50:57], v[26:33], v[162:165], v218, v218 op_sel_hi:[0,0,0]
	v_mfma_scale_f32_16x16x128_f8f6f4 v[158:161], v[50:57], v[18:25], v[158:161], v218, v218 op_sel_hi:[0,0,0]
	v_mfma_scale_f32_16x16x128_f8f6f4 v[154:157], v[50:57], v[10:17], v[154:157], v218, v218 op_sel_hi:[0,0,0]
	v_mfma_scale_f32_16x16x128_f8f6f4 v[150:153], v[50:57], v[2:9], v[150:153], v218, v218 op_sel_hi:[0,0,0]
	v_mfma_scale_f32_16x16x128_f8f6f4 v[146:149], v[34:41], v[26:33], v[146:149], v218, v218 op_sel_hi:[0,0,0]
	v_mfma_scale_f32_16x16x128_f8f6f4 v[142:145], v[34:41], v[18:25], v[142:145], v218, v218 op_sel_hi:[0,0,0]
	v_mfma_scale_f32_16x16x128_f8f6f4 v[138:141], v[34:41], v[10:17], v[138:141], v218, v218 op_sel_hi:[0,0,0]
	v_mfma_scale_f32_16x16x128_f8f6f4 v[134:137], v[34:41], v[2:9], v[134:137], v218, v218 op_sel_hi:[0,0,0]
	ds_read_b128 v[50:53], v68 offset:12288
	ds_read_b128 v[54:57], v66 offset:12288
	ds_read_b128 v[34:37], v68 offset:14336
	ds_read_b128 v[38:41], v66 offset:14336
	s_waitcnt lgkmcnt(4)
	v_mfma_scale_f32_16x16x128_f8f6f4 v[130:133], v[58:65], v[26:33], v[130:133], v218, v218 op_sel_hi:[0,0,0]
	v_mfma_scale_f32_16x16x128_f8f6f4 v[126:129], v[58:65], v[18:25], v[126:129], v218, v218 op_sel_hi:[0,0,0]
	v_mfma_scale_f32_16x16x128_f8f6f4 v[122:125], v[58:65], v[10:17], v[122:125], v218, v218 op_sel_hi:[0,0,0]
	v_mfma_scale_f32_16x16x128_f8f6f4 v[118:121], v[58:65], v[2:9], v[118:121], v218, v218 op_sel_hi:[0,0,0]
	v_mfma_scale_f32_16x16x128_f8f6f4 v[114:117], v[42:49], v[26:33], v[114:117], v218, v218 op_sel_hi:[0,0,0]
	v_mfma_scale_f32_16x16x128_f8f6f4 v[110:113], v[42:49], v[18:25], v[110:113], v218, v218 op_sel_hi:[0,0,0]
	v_mfma_scale_f32_16x16x128_f8f6f4 v[106:109], v[42:49], v[10:17], v[106:109], v218, v218 op_sel_hi:[0,0,0]
	v_mfma_scale_f32_16x16x128_f8f6f4 v[102:105], v[42:49], v[2:9], v[102:105], v218, v218 op_sel_hi:[0,0,0]
	s_waitcnt lgkmcnt(0)
	v_mfma_scale_f32_16x16x128_f8f6f4 v[98:101], v[50:57], v[26:33], v[98:101], v218, v218 op_sel_hi:[0,0,0]
	v_mfma_scale_f32_16x16x128_f8f6f4 v[94:97], v[50:57], v[18:25], v[94:97], v218, v218 op_sel_hi:[0,0,0]
	v_mfma_scale_f32_16x16x128_f8f6f4 v[90:93], v[50:57], v[10:17], v[90:93], v218, v218 op_sel_hi:[0,0,0]
	v_mfma_scale_f32_16x16x128_f8f6f4 v[86:89], v[50:57], v[2:9], v[86:89], v218, v218 op_sel_hi:[0,0,0]
	v_mfma_scale_f32_16x16x128_f8f6f4 v[82:85], v[34:41], v[26:33], v[82:85], v218, v218 op_sel_hi:[0,0,0]
	v_mfma_scale_f32_16x16x128_f8f6f4 v[78:81], v[34:41], v[18:25], v[78:81], v218, v218 op_sel_hi:[0,0,0]
	v_mfma_scale_f32_16x16x128_f8f6f4 v[74:77], v[34:41], v[10:17], v[74:77], v218, v218 op_sel_hi:[0,0,0]
	v_mfma_scale_f32_16x16x128_f8f6f4 v[70:73], v[34:41], v[2:9], v[70:73], v218, v218 op_sel_hi:[0,0,0]
	s_branch .LBB0_225
.Lp1b_XT:
	s_and_b32 s5, s4, 0x10000
	v_or_b32_e32 v2, s5, v250
	v_xor_b32_e32 v6, 64, v2
	v_add_u32_e32 v68, s5, v249
	v_xor_b32_e32 v66, 64, v68
	ds_read_b128 v[26:29], v2 offset:0
	ds_read_b128 v[30:33], v6 offset:0
	ds_read_b128 v[58:61], v68 offset:0
	ds_read_b128 v[62:65], v66 offset:0
	ds_read_b128 v[18:21], v2 offset:2048
	ds_read_b128 v[22:25], v6 offset:2048
	ds_read_b128 v[10:13], v2 offset:4096
	ds_read_b128 v[14:17], v6 offset:4096
	ds_read_b128 v[2:5], v2 offset:6144
	ds_read_b128 v[6:9], v6 offset:6144
	ds_read_b128 v[42:45], v68 offset:2048
	ds_read_b128 v[46:49], v66 offset:2048
	ds_read_b128 v[50:53], v68 offset:4096
	ds_read_b128 v[54:57], v66 offset:4096
	ds_read_b128 v[34:37], v68 offset:6144
	ds_read_b128 v[38:41], v66 offset:6144
	s_nop 0
	s_waitcnt lgkmcnt(12)
	v_mfma_scale_f32_16x16x128_f8f6f4 v[194:197], v[26:33], v[58:65], v[194:197], v218, v218 op_sel_hi:[0,0,0]
	s_waitcnt lgkmcnt(10)
	v_mfma_scale_f32_16x16x128_f8f6f4 v[190:193], v[18:25], v[58:65], v[190:193], v218, v218 op_sel_hi:[0,0,0]
	s_waitcnt lgkmcnt(8)
	v_mfma_scale_f32_16x16x128_f8f6f4 v[186:189], v[10:17], v[58:65], v[186:189], v218, v218 op_sel_hi:[0,0,0]
	s_waitcnt lgkmcnt(6)
	v_mfma_scale_f32_16x16x128_f8f6f4 v[182:185], v[2:9], v[58:65], v[182:185], v218, v218 op_sel_hi:[0,0,0]
	s_waitcnt lgkmcnt(4)
	v_mfma_scale_f32_16x16x128_f8f6f4 v[178:181], v[26:33], v[42:49], v[178:181], v218, v218 op_sel_hi:[0,0,0]
	v_mfma_scale_f32_16x16x128_f8f6f4 v[174:177], v[18:25], v[42:49], v[174:177], v218, v218 op_sel_hi:[0,0,0]
	v_mfma_scale_f32_16x16x128_f8f6f4 v[170:173], v[10:17], v[42:49], v[170:173], v218, v218 op_sel_hi:[0,0,0]
	v_mfma_scale_f32_16x16x128_f8f6f4 v[166:169], v[2:9], v[42:49], v[166:169], v218, v218 op_sel_hi:[0,0,0]
	ds_read_b128 v[58:61], v68 offset:8192
	ds_read_b128 v[62:65], v66 offset:8192
	ds_read_b128 v[42:45], v68 offset:10240
	ds_read_b128 v[46:49], v66 offset:10240
	s_waitcnt lgkmcnt(4)
	v_mfma_scale_f32_16x16x128_f8f6f4 v[162:165], v[26:33], v[50:57], v[162:165], v218, v218 op_sel_hi:[0,0,0]
	v_mfma_scale_f32_16x16x128_f8f6f4 v[158:161], v[18:25], v[50:57], v[158:161], v218, v218 op_sel_hi:[0,0,0]
	v_mfma_scale_f32_16x16x128_f8f6f4 v[154:157], v[10:17], v[50:57], v[154:157], v218, v218 op_sel_hi:[0,0,0]
	v_mfma_scale_f32_16x16x128_f8f6f4 v[150:153], v[2:9], v[50:57], v[150:153], v218, v218 op_sel_hi:[0,0,0]
	v_mfma_scale_f32_16x16x128_f8f6f4 v[146:149], v[26:33], v[34:41], v[146:149], v218, v218 op_sel_hi:[0,0,0]
	v_mfma_scale_f32_16x16x128_f8f6f4 v[142:145], v[18:25], v[34:41], v[142:145], v218, v218 op_sel_hi:[0,0,0]
	v_mfma_scale_f32_16x16x128_f8f6f4 v[138:141], v[10:17], v[34:41], v[138:141], v218, v218 op_sel_hi:[0,0,0]
	v_mfma_scale_f32_16x16x128_f8f6f4 v[134:137], v[2:9], v[34:41], v[134:137], v218, v218 op_sel_hi:[0,0,0]
	ds_read_b128 v[50:53], v68 offset:12288
	ds_read_b128 v[54:57], v66 offset:12288
	ds_read_b128 v[34:37], v68 offset:14336
	ds_read_b128 v[38:41], v66 offset:14336
	s_waitcnt lgkmcnt(4)
	v_mfma_scale_f32_16x16x128_f8f6f4 v[130:133], v[26:33], v[58:65], v[130:133], v218, v218 op_sel_hi:[0,0,0]
	v_mfma_scale_f32_16x16x128_f8f6f4 v[126:129], v[18:25], v[58:65], v[126:129], v218, v218 op_sel_hi:[0,0,0]
	v_mfma_scale_f32_16x16x128_f8f6f4 v[122:125], v[10:17], v[58:65], v[122:125], v218, v218 op_sel_hi:[0,0,0]
	v_mfma_scale_f32_16x16x128_f8f6f4 v[118:121], v[2:9], v[58:65], v[118:121], v218, v218 op_sel_hi:[0,0,0]
	v_mfma_scale_f32_16x16x128_f8f6f4 v[114:117], v[26:33], v[42:49], v[114:117], v218, v218 op_sel_hi:[0,0,0]
	v_mfma_scale_f32_16x16x128_f8f6f4 v[110:113], v[18:25], v[42:49], v[110:113], v218, v218 op_sel_hi:[0,0,0]
	v_mfma_scale_f32_16x16x128_f8f6f4 v[106:109], v[10:17], v[42:49], v[106:109], v218, v218 op_sel_hi:[0,0,0]
	v_mfma_scale_f32_16x16x128_f8f6f4 v[102:105], v[2:9], v[42:49], v[102:105], v218, v218 op_sel_hi:[0,0,0]
	s_waitcnt lgkmcnt(0)
	v_mfma_scale_f32_16x16x128_f8f6f4 v[98:101], v[26:33], v[50:57], v[98:101], v218, v218 op_sel_hi:[0,0,0]
	v_mfma_scale_f32_16x16x128_f8f6f4 v[94:97], v[18:25], v[50:57], v[94:97], v218, v218 op_sel_hi:[0,0,0]
	v_mfma_scale_f32_16x16x128_f8f6f4 v[90:93], v[10:17], v[50:57], v[90:93], v218, v218 op_sel_hi:[0,0,0]
	v_mfma_scale_f32_16x16x128_f8f6f4 v[86:89], v[2:9], v[50:57], v[86:89], v218, v218 op_sel_hi:[0,0,0]
	v_mfma_scale_f32_16x16x128_f8f6f4 v[82:85], v[26:33], v[34:41], v[82:85], v218, v218 op_sel_hi:[0,0,0]
	v_mfma_scale_f32_16x16x128_f8f6f4 v[78:81], v[18:25], v[34:41], v[78:81], v218, v218 op_sel_hi:[0,0,0]
	v_mfma_scale_f32_16x16x128_f8f6f4 v[74:77], v[10:17], v[34:41], v[74:77], v218, v218 op_sel_hi:[0,0,0]
	v_mfma_scale_f32_16x16x128_f8f6f4 v[70:73], v[2:9], v[34:41], v[70:73], v218, v218 op_sel_hi:[0,0,0]
	s_branch .LBB0_225

.LBB0_515:
	s_add_i32 s26, s39, s5
	s_and_b32 s26, s26, 0x10000
	v_add_u32_e32 v2, s26, v249
	v_xor_b32_e32 v156, 64, v2
	v_or_b32_e32 v157, s26, v250
	v_xor_b32_e32 v158, 64, v157
	ds_read_b128 v[132:135], v157 offset:0
	ds_read_b128 v[136:139], v158 offset:0
	ds_read_b128 v[204:207], v2 offset:0
	ds_read_b128 v[208:211], v156 offset:0
	ds_read_b128 v[140:143], v157 offset:0x800
	ds_read_b128 v[144:147], v158 offset:0x800
	ds_read_b128 v[148:151], v157 offset:0x1000
	ds_read_b128 v[152:155], v158 offset:0x1000
	ds_read_b128 v[176:179], v157 offset:0x1800
	ds_read_b128 v[180:183], v158 offset:0x1800
	ds_read_b128 v[216:219], v2 offset:0x800
	ds_read_b128 v[220:223], v156 offset:0x800
	ds_read_b128 v[224:227], v2 offset:0x1000
	ds_read_b128 v[228:231], v156 offset:0x1000
	ds_read_b128 v[232:235], v2 offset:0x1800
	ds_read_b128 v[236:239], v156 offset:0x1800
	s_nop 0
	s_waitcnt lgkmcnt(12)
	v_mfma_scale_f32_16x16x128_f8f6f4 v[4:7], v[132:139], v[204:211], v[4:7], v203, v203 op_sel_hi:[0,0,0]
	s_waitcnt lgkmcnt(10)
	v_mfma_scale_f32_16x16x128_f8f6f4 v[128:131], v[140:147], v[204:211], v[128:131], v203, v203 op_sel_hi:[0,0,0]
	s_waitcnt lgkmcnt(8)
	v_mfma_scale_f32_16x16x128_f8f6f4 v[124:127], v[148:155], v[204:211], v[124:127], v203, v203 op_sel_hi:[0,0,0]
	s_waitcnt lgkmcnt(6)
	v_mfma_scale_f32_16x16x128_f8f6f4 v[120:123], v[176:183], v[204:211], v[120:123], v203, v203 op_sel_hi:[0,0,0]
	s_waitcnt lgkmcnt(4)
	v_mfma_scale_f32_16x16x128_f8f6f4 v[100:103], v[132:139], v[216:223], v[100:103], v203, v203 op_sel_hi:[0,0,0]
	v_mfma_scale_f32_16x16x128_f8f6f4 v[104:107], v[140:147], v[216:223], v[104:107], v203, v203 op_sel_hi:[0,0,0]
	v_mfma_scale_f32_16x16x128_f8f6f4 v[108:111], v[148:155], v[216:223], v[108:111], v203, v203 op_sel_hi:[0,0,0]
	v_mfma_scale_f32_16x16x128_f8f6f4 v[112:115], v[176:183], v[216:223], v[112:115], v203, v203 op_sel_hi:[0,0,0]
	ds_read_b128 v[204:207], v2 offset:0x2000
	ds_read_b128 v[208:211], v156 offset:0x2000
	ds_read_b128 v[216:219], v2 offset:0x2800
	ds_read_b128 v[220:223], v156 offset:0x2800
	s_waitcnt lgkmcnt(4)
	v_mfma_scale_f32_16x16x128_f8f6f4 v[84:87], v[132:139], v[224:231], v[84:87], v203, v203 op_sel_hi:[0,0,0]
	v_mfma_scale_f32_16x16x128_f8f6f4 v[88:91], v[140:147], v[224:231], v[88:91], v203, v203 op_sel_hi:[0,0,0]
	v_mfma_scale_f32_16x16x128_f8f6f4 v[92:95], v[148:155], v[224:231], v[92:95], v203, v203 op_sel_hi:[0,0,0]
	v_mfma_scale_f32_16x16x128_f8f6f4 v[96:99], v[176:183], v[224:231], v[96:99], v203, v203 op_sel_hi:[0,0,0]
	v_mfma_scale_f32_16x16x128_f8f6f4 v[68:71], v[132:139], v[232:239], v[68:71], v203, v203 op_sel_hi:[0,0,0]
	v_mfma_scale_f32_16x16x128_f8f6f4 v[72:75], v[140:147], v[232:239], v[72:75], v203, v203 op_sel_hi:[0,0,0]
	v_mfma_scale_f32_16x16x128_f8f6f4 v[76:79], v[148:155], v[232:239], v[76:79], v203, v203 op_sel_hi:[0,0,0]
	v_mfma_scale_f32_16x16x128_f8f6f4 v[80:83], v[176:183], v[232:239], v[80:83], v203, v203 op_sel_hi:[0,0,0]
	ds_read_b128 v[224:227], v2 offset:0x3000
	ds_read_b128 v[228:231], v156 offset:0x3000
	ds_read_b128 v[232:235], v2 offset:0x3800
	ds_read_b128 v[236:239], v156 offset:0x3800
	s_waitcnt lgkmcnt(4)
	v_mfma_scale_f32_16x16x128_f8f6f4 v[52:55], v[132:139], v[204:211], v[52:55], v203, v203 op_sel_hi:[0,0,0]
	v_mfma_scale_f32_16x16x128_f8f6f4 v[56:59], v[140:147], v[204:211], v[56:59], v203, v203 op_sel_hi:[0,0,0]
	v_mfma_scale_f32_16x16x128_f8f6f4 v[60:63], v[148:155], v[204:211], v[60:63], v203, v203 op_sel_hi:[0,0,0]
	v_mfma_scale_f32_16x16x128_f8f6f4 v[64:67], v[176:183], v[204:211], v[64:67], v203, v203 op_sel_hi:[0,0,0]
	v_mfma_scale_f32_16x16x128_f8f6f4 v[36:39], v[132:139], v[216:223], v[36:39], v203, v203 op_sel_hi:[0,0,0]
	v_mfma_scale_f32_16x16x128_f8f6f4 v[40:43], v[140:147], v[216:223], v[40:43], v203, v203 op_sel_hi:[0,0,0]
	v_mfma_scale_f32_16x16x128_f8f6f4 v[44:47], v[148:155], v[216:223], v[44:47], v203, v203 op_sel_hi:[0,0,0]
	v_mfma_scale_f32_16x16x128_f8f6f4 v[48:51], v[176:183], v[216:223], v[48:51], v203, v203 op_sel_hi:[0,0,0]
	s_waitcnt lgkmcnt(0)
	v_mfma_scale_f32_16x16x128_f8f6f4 v[20:23], v[132:139], v[224:231], v[20:23], v203, v203 op_sel_hi:[0,0,0]
	v_mfma_scale_f32_16x16x128_f8f6f4 v[24:27], v[140:147], v[224:231], v[24:27], v203, v203 op_sel_hi:[0,0,0]
	v_mfma_scale_f32_16x16x128_f8f6f4 v[28:31], v[148:155], v[224:231], v[28:31], v203, v203 op_sel_hi:[0,0,0]
	v_mfma_scale_f32_16x16x128_f8f6f4 v[32:35], v[176:183], v[224:231], v[32:35], v203, v203 op_sel_hi:[0,0,0]
	v_mfma_scale_f32_16x16x128_f8f6f4 v[116:119], v[132:139], v[232:239], v[116:119], v203, v203 op_sel_hi:[0,0,0]
	v_mfma_scale_f32_16x16x128_f8f6f4 v[8:11], v[140:147], v[232:239], v[8:11], v203, v203 op_sel_hi:[0,0,0]
	v_mfma_scale_f32_16x16x128_f8f6f4 v[12:15], v[148:155], v[232:239], v[12:15], v203, v203 op_sel_hi:[0,0,0]
	v_mfma_scale_f32_16x16x128_f8f6f4 v[16:19], v[176:183], v[232:239], v[16:19], v203, v203 op_sel_hi:[0,0,0]
	s_branch .LBB0_501

.LBB0_530:
	s_add_i32 s26, s30, s31
	s_and_b32 s26, s26, 0x10000
	v_add_u32_e32 v2, s26, v249
	v_xor_b32_e32 v116, 64, v2
	v_or_b32_e32 v117, s26, v250
	v_xor_b32_e32 v118, 64, v117
	ds_read_b128 v[136:139], v117 offset:0
	ds_read_b128 v[140:143], v118 offset:0
	ds_read_b128 v[204:207], v2 offset:0
	ds_read_b128 v[208:211], v116 offset:0
	ds_read_b128 v[144:147], v117 offset:0x800
	ds_read_b128 v[148:151], v118 offset:0x800
	ds_read_b128 v[152:155], v117 offset:0x1000
	ds_read_b128 v[156:159], v118 offset:0x1000
	ds_read_b128 v[176:179], v117 offset:0x1800
	ds_read_b128 v[180:183], v118 offset:0x1800
	ds_read_b128 v[216:219], v2 offset:0x800
	ds_read_b128 v[220:223], v116 offset:0x800
	ds_read_b128 v[224:227], v2 offset:0x1000
	ds_read_b128 v[228:231], v116 offset:0x1000
	ds_read_b128 v[232:235], v2 offset:0x1800
	ds_read_b128 v[236:239], v116 offset:0x1800
	s_nop 0
	s_waitcnt lgkmcnt(12)
	v_mfma_scale_f32_16x16x128_f8f6f4 v[132:135], v[136:143], v[204:211], v[132:135], v203, v203 op_sel_hi:[0,0,0]
	s_waitcnt lgkmcnt(10)
	v_mfma_scale_f32_16x16x128_f8f6f4 v[128:131], v[144:151], v[204:211], v[128:131], v203, v203 op_sel_hi:[0,0,0]
	s_waitcnt lgkmcnt(8)
	v_mfma_scale_f32_16x16x128_f8f6f4 v[124:127], v[152:159], v[204:211], v[124:127], v203, v203 op_sel_hi:[0,0,0]
	s_waitcnt lgkmcnt(6)
	v_mfma_scale_f32_16x16x128_f8f6f4 v[120:123], v[176:183], v[204:211], v[120:123], v203, v203 op_sel_hi:[0,0,0]
	s_waitcnt lgkmcnt(4)
	v_mfma_scale_f32_16x16x128_f8f6f4 v[100:103], v[136:143], v[216:223], v[100:103], v203, v203 op_sel_hi:[0,0,0]
	v_mfma_scale_f32_16x16x128_f8f6f4 v[104:107], v[144:151], v[216:223], v[104:107], v203, v203 op_sel_hi:[0,0,0]
	v_mfma_scale_f32_16x16x128_f8f6f4 v[108:111], v[152:159], v[216:223], v[108:111], v203, v203 op_sel_hi:[0,0,0]
	v_mfma_scale_f32_16x16x128_f8f6f4 v[112:115], v[176:183], v[216:223], v[112:115], v203, v203 op_sel_hi:[0,0,0]
	ds_read_b128 v[204:207], v2 offset:0x2000
	ds_read_b128 v[208:211], v116 offset:0x2000
	ds_read_b128 v[216:219], v2 offset:0x2800
	ds_read_b128 v[220:223], v116 offset:0x2800
	s_waitcnt lgkmcnt(4)
	v_mfma_scale_f32_16x16x128_f8f6f4 v[84:87], v[136:143], v[224:231], v[84:87], v203, v203 op_sel_hi:[0,0,0]
	v_mfma_scale_f32_16x16x128_f8f6f4 v[88:91], v[144:151], v[224:231], v[88:91], v203, v203 op_sel_hi:[0,0,0]
	v_mfma_scale_f32_16x16x128_f8f6f4 v[92:95], v[152:159], v[224:231], v[92:95], v203, v203 op_sel_hi:[0,0,0]
	v_mfma_scale_f32_16x16x128_f8f6f4 v[96:99], v[176:183], v[224:231], v[96:99], v203, v203 op_sel_hi:[0,0,0]
	v_mfma_scale_f32_16x16x128_f8f6f4 v[68:71], v[136:143], v[232:239], v[68:71], v203, v203 op_sel_hi:[0,0,0]
	v_mfma_scale_f32_16x16x128_f8f6f4 v[72:75], v[144:151], v[232:239], v[72:75], v203, v203 op_sel_hi:[0,0,0]
	v_mfma_scale_f32_16x16x128_f8f6f4 v[76:79], v[152:159], v[232:239], v[76:79], v203, v203 op_sel_hi:[0,0,0]
	v_mfma_scale_f32_16x16x128_f8f6f4 v[80:83], v[176:183], v[232:239], v[80:83], v203, v203 op_sel_hi:[0,0,0]
	ds_read_b128 v[224:227], v2 offset:0x3000
	ds_read_b128 v[228:231], v116 offset:0x3000
	ds_read_b128 v[232:235], v2 offset:0x3800
	ds_read_b128 v[236:239], v116 offset:0x3800
	s_waitcnt lgkmcnt(4)
	v_mfma_scale_f32_16x16x128_f8f6f4 v[52:55], v[136:143], v[204:211], v[52:55], v203, v203 op_sel_hi:[0,0,0]
	v_mfma_scale_f32_16x16x128_f8f6f4 v[56:59], v[144:151], v[204:211], v[56:59], v203, v203 op_sel_hi:[0,0,0]
	v_mfma_scale_f32_16x16x128_f8f6f4 v[60:63], v[152:159], v[204:211], v[60:63], v203, v203 op_sel_hi:[0,0,0]
	v_mfma_scale_f32_16x16x128_f8f6f4 v[64:67], v[176:183], v[204:211], v[64:67], v203, v203 op_sel_hi:[0,0,0]
	v_mfma_scale_f32_16x16x128_f8f6f4 v[36:39], v[136:143], v[216:223], v[36:39], v203, v203 op_sel_hi:[0,0,0]
	v_mfma_scale_f32_16x16x128_f8f6f4 v[40:43], v[144:151], v[216:223], v[40:43], v203, v203 op_sel_hi:[0,0,0]
	v_mfma_scale_f32_16x16x128_f8f6f4 v[44:47], v[152:159], v[216:223], v[44:47], v203, v203 op_sel_hi:[0,0,0]
	v_mfma_scale_f32_16x16x128_f8f6f4 v[48:51], v[176:183], v[216:223], v[48:51], v203, v203 op_sel_hi:[0,0,0]
	s_waitcnt lgkmcnt(0)
	v_mfma_scale_f32_16x16x128_f8f6f4 v[20:23], v[136:143], v[224:231], v[20:23], v203, v203 op_sel_hi:[0,0,0]
	v_mfma_scale_f32_16x16x128_f8f6f4 v[24:27], v[144:151], v[224:231], v[24:27], v203, v203 op_sel_hi:[0,0,0]
	v_mfma_scale_f32_16x16x128_f8f6f4 v[28:31], v[152:159], v[224:231], v[28:31], v203, v203 op_sel_hi:[0,0,0]
	v_mfma_scale_f32_16x16x128_f8f6f4 v[32:35], v[176:183], v[224:231], v[32:35], v203, v203 op_sel_hi:[0,0,0]
	v_mfma_scale_f32_16x16x128_f8f6f4 v[4:7], v[136:143], v[232:239], v[4:7], v203, v203 op_sel_hi:[0,0,0]
	v_mfma_scale_f32_16x16x128_f8f6f4 v[8:11], v[144:151], v[232:239], v[8:11], v203, v203 op_sel_hi:[0,0,0]
	v_mfma_scale_f32_16x16x128_f8f6f4 v[12:15], v[152:159], v[232:239], v[12:15], v203, v203 op_sel_hi:[0,0,0]
	v_mfma_scale_f32_16x16x128_f8f6f4 v[16:19], v[176:183], v[232:239], v[16:19], v203, v203 op_sel_hi:[0,0,0]
	s_branch .LBB0_517

.LBB0_790:
	s_and_b32 s11, s36, 0x10000
	v_add_u32_e32 v2, s11, v249
	v_xor_b32_e32 v4, 64, v2
	v_or_b32_e32 v5, s11, v250
	v_xor_b32_e32 v163, 64, v5
	ds_read_b128 v[150:153], v5 offset:0
	ds_read_b128 v[154:157], v163 offset:0
	ds_read_b128 v[188:191], v2 offset:0
	ds_read_b128 v[192:195], v4 offset:0
	ds_read_b128 v[164:167], v5 offset:0x800
	ds_read_b128 v[168:171], v163 offset:0x800
	ds_read_b128 v[172:175], v5 offset:0x1000
	ds_read_b128 v[176:179], v163 offset:0x1000
	ds_read_b128 v[180:183], v5 offset:0x1800
	ds_read_b128 v[184:187], v163 offset:0x1800
	ds_read_b128 v[196:199], v2 offset:0x800
	ds_read_b128 v[200:203], v4 offset:0x800
	ds_read_b128 v[204:207], v2 offset:0x1000
	ds_read_b128 v[208:211], v4 offset:0x1000
	ds_read_b128 v[216:219], v2 offset:0x1800
	ds_read_b128 v[220:223], v4 offset:0x1800
	s_nop 0
	s_waitcnt lgkmcnt(12)
	v_mfma_scale_f32_16x16x128_f8f6f4 v[130:133], v[150:157], v[188:195], v[130:133], v161, v161 op_sel_hi:[0,0,0]
	s_waitcnt lgkmcnt(10)
	v_mfma_scale_f32_16x16x128_f8f6f4 v[122:125], v[164:171], v[188:195], v[122:125], v161, v161 op_sel_hi:[0,0,0]
	s_waitcnt lgkmcnt(8)
	v_mfma_scale_f32_16x16x128_f8f6f4 v[126:129], v[172:179], v[188:195], v[126:129], v161, v161 op_sel_hi:[0,0,0]
	s_waitcnt lgkmcnt(6)
	v_mfma_scale_f32_16x16x128_f8f6f4 v[118:121], v[180:187], v[188:195], v[118:121], v161, v161 op_sel_hi:[0,0,0]
	s_waitcnt lgkmcnt(4)
	v_mfma_scale_f32_16x16x128_f8f6f4 v[114:117], v[150:157], v[196:203], v[114:117], v161, v161 op_sel_hi:[0,0,0]
	v_mfma_scale_f32_16x16x128_f8f6f4 v[106:109], v[164:171], v[196:203], v[106:109], v161, v161 op_sel_hi:[0,0,0]
	v_mfma_scale_f32_16x16x128_f8f6f4 v[110:113], v[172:179], v[196:203], v[110:113], v161, v161 op_sel_hi:[0,0,0]
	v_mfma_scale_f32_16x16x128_f8f6f4 v[102:105], v[180:187], v[196:203], v[102:105], v161, v161 op_sel_hi:[0,0,0]
	ds_read_b128 v[188:191], v2 offset:0x2000
	ds_read_b128 v[192:195], v4 offset:0x2000
	ds_read_b128 v[196:199], v2 offset:0x2800
	ds_read_b128 v[200:203], v4 offset:0x2800
	s_waitcnt lgkmcnt(4)
	v_mfma_scale_f32_16x16x128_f8f6f4 v[98:101], v[150:157], v[204:211], v[98:101], v161, v161 op_sel_hi:[0,0,0]
	v_mfma_scale_f32_16x16x128_f8f6f4 v[90:93], v[164:171], v[204:211], v[90:93], v161, v161 op_sel_hi:[0,0,0]
	v_mfma_scale_f32_16x16x128_f8f6f4 v[94:97], v[172:179], v[204:211], v[94:97], v161, v161 op_sel_hi:[0,0,0]
	v_mfma_scale_f32_16x16x128_f8f6f4 v[86:89], v[180:187], v[204:211], v[86:89], v161, v161 op_sel_hi:[0,0,0]
	v_mfma_scale_f32_16x16x128_f8f6f4 v[82:85], v[150:157], v[216:223], v[82:85], v161, v161 op_sel_hi:[0,0,0]
	v_mfma_scale_f32_16x16x128_f8f6f4 v[74:77], v[164:171], v[216:223], v[74:77], v161, v161 op_sel_hi:[0,0,0]
	v_mfma_scale_f32_16x16x128_f8f6f4 v[78:81], v[172:179], v[216:223], v[78:81], v161, v161 op_sel_hi:[0,0,0]
	v_mfma_scale_f32_16x16x128_f8f6f4 v[70:73], v[180:187], v[216:223], v[70:73], v161, v161 op_sel_hi:[0,0,0]
	ds_read_b128 v[204:207], v2 offset:0x3000
	ds_read_b128 v[208:211], v4 offset:0x3000
	ds_read_b128 v[216:219], v2 offset:0x3800
	ds_read_b128 v[220:223], v4 offset:0x3800
	s_waitcnt lgkmcnt(4)
	v_mfma_scale_f32_16x16x128_f8f6f4 v[66:69], v[150:157], v[188:195], v[66:69], v161, v161 op_sel_hi:[0,0,0]
	v_mfma_scale_f32_16x16x128_f8f6f4 v[58:61], v[164:171], v[188:195], v[58:61], v161, v161 op_sel_hi:[0,0,0]
	v_mfma_scale_f32_16x16x128_f8f6f4 v[62:65], v[172:179], v[188:195], v[62:65], v161, v161 op_sel_hi:[0,0,0]
	v_mfma_scale_f32_16x16x128_f8f6f4 v[54:57], v[180:187], v[188:195], v[54:57], v161, v161 op_sel_hi:[0,0,0]
	v_mfma_scale_f32_16x16x128_f8f6f4 v[50:53], v[150:157], v[196:203], v[50:53], v161, v161 op_sel_hi:[0,0,0]
	v_mfma_scale_f32_16x16x128_f8f6f4 v[42:45], v[164:171], v[196:203], v[42:45], v161, v161 op_sel_hi:[0,0,0]
	v_mfma_scale_f32_16x16x128_f8f6f4 v[46:49], v[172:179], v[196:203], v[46:49], v161, v161 op_sel_hi:[0,0,0]
	v_mfma_scale_f32_16x16x128_f8f6f4 v[38:41], v[180:187], v[196:203], v[38:41], v161, v161 op_sel_hi:[0,0,0]
	s_waitcnt lgkmcnt(0)
	v_mfma_scale_f32_16x16x128_f8f6f4 v[34:37], v[150:157], v[204:211], v[34:37], v161, v161 op_sel_hi:[0,0,0]
	v_mfma_scale_f32_16x16x128_f8f6f4 v[26:29], v[164:171], v[204:211], v[26:29], v161, v161 op_sel_hi:[0,0,0]
	v_mfma_scale_f32_16x16x128_f8f6f4 v[30:33], v[172:179], v[204:211], v[30:33], v161, v161 op_sel_hi:[0,0,0]
	v_mfma_scale_f32_16x16x128_f8f6f4 v[22:25], v[180:187], v[204:211], v[22:25], v161, v161 op_sel_hi:[0,0,0]
	v_mfma_scale_f32_16x16x128_f8f6f4 v[18:21], v[150:157], v[216:223], v[18:21], v161, v161 op_sel_hi:[0,0,0]
	v_mfma_scale_f32_16x16x128_f8f6f4 v[10:13], v[164:171], v[216:223], v[10:13], v161, v161 op_sel_hi:[0,0,0]
	v_mfma_scale_f32_16x16x128_f8f6f4 v[14:17], v[172:179], v[216:223], v[14:17], v161, v161 op_sel_hi:[0,0,0]
	v_mfma_scale_f32_16x16x128_f8f6f4 v[6:9], v[180:187], v[216:223], v[6:9], v161, v161 op_sel_hi:[0,0,0]
	s_branch .LBB0_768

.LBB0_1050:
	s_cmp_lt_u32 s4, 0x4000
	s_cbranch_scc0 .Lp5a_ybody
	s_and_b32 s13, s31, 0x10000
	v_add_u32_e32 v2, s13, v249
	v_xor_b32_e32 v4, 64, v2
	v_or_b32_e32 v5, s13, v250
	v_xor_b32_e32 v166, 64, v5
	ds_read_b128 v[158:161], v5 offset:0
	ds_read_b128 v[162:165], v166 offset:0
	ds_read_b128 v[206:209], v2 offset:0
	ds_read_b128 v[210:213], v4 offset:0
	ds_read_b128 v[182:185], v5 offset:0x800
	ds_read_b128 v[186:189], v166 offset:0x800
	ds_read_b128 v[190:193], v5 offset:0x1000
	ds_read_b128 v[194:197], v166 offset:0x1000
	ds_read_b128 v[198:201], v5 offset:0x1800
	ds_read_b128 v[202:205], v166 offset:0x1800
	ds_read_b128 v[214:217], v2 offset:0x800
	ds_read_b128 v[218:221], v4 offset:0x800
	ds_read_b128 v[222:225], v2 offset:0x1000
	ds_read_b128 v[226:229], v4 offset:0x1000
	ds_read_b128 v[230:233], v2 offset:0x1800
	ds_read_b128 v[234:237], v4 offset:0x1800
	s_nop 0
	s_waitcnt lgkmcnt(12)
	v_mfma_scale_f32_16x16x128_f8f6f4 v[130:133], v[158:165], v[206:213], v[130:133], v178, v178 op_sel_hi:[0,0,0]
	s_waitcnt lgkmcnt(10)
	v_mfma_scale_f32_16x16x128_f8f6f4 v[122:125], v[182:189], v[206:213], v[122:125], v178, v178 op_sel_hi:[0,0,0]
	s_waitcnt lgkmcnt(8)
	v_mfma_scale_f32_16x16x128_f8f6f4 v[126:129], v[190:197], v[206:213], v[126:129], v178, v178 op_sel_hi:[0,0,0]
	s_waitcnt lgkmcnt(6)
	v_mfma_scale_f32_16x16x128_f8f6f4 v[118:121], v[198:205], v[206:213], v[118:121], v178, v178 op_sel_hi:[0,0,0]
	s_waitcnt lgkmcnt(4)
	v_mfma_scale_f32_16x16x128_f8f6f4 v[114:117], v[158:165], v[214:221], v[114:117], v178, v178 op_sel_hi:[0,0,0]
	v_mfma_scale_f32_16x16x128_f8f6f4 v[106:109], v[182:189], v[214:221], v[106:109], v178, v178 op_sel_hi:[0,0,0]
	v_mfma_scale_f32_16x16x128_f8f6f4 v[110:113], v[190:197], v[214:221], v[110:113], v178, v178 op_sel_hi:[0,0,0]
	v_mfma_scale_f32_16x16x128_f8f6f4 v[102:105], v[198:205], v[214:221], v[102:105], v178, v178 op_sel_hi:[0,0,0]
	ds_read_b128 v[206:209], v2 offset:0x2000
	ds_read_b128 v[210:213], v4 offset:0x2000
	ds_read_b128 v[214:217], v2 offset:0x2800
	ds_read_b128 v[218:221], v4 offset:0x2800
	s_waitcnt lgkmcnt(4)
	v_mfma_scale_f32_16x16x128_f8f6f4 v[98:101], v[158:165], v[222:229], v[98:101], v178, v178 op_sel_hi:[0,0,0]
	v_mfma_scale_f32_16x16x128_f8f6f4 v[90:93], v[182:189], v[222:229], v[90:93], v178, v178 op_sel_hi:[0,0,0]
	v_mfma_scale_f32_16x16x128_f8f6f4 v[94:97], v[190:197], v[222:229], v[94:97], v178, v178 op_sel_hi:[0,0,0]
	v_mfma_scale_f32_16x16x128_f8f6f4 v[86:89], v[198:205], v[222:229], v[86:89], v178, v178 op_sel_hi:[0,0,0]
	v_mfma_scale_f32_16x16x128_f8f6f4 v[82:85], v[158:165], v[230:237], v[82:85], v178, v178 op_sel_hi:[0,0,0]
	v_mfma_scale_f32_16x16x128_f8f6f4 v[74:77], v[182:189], v[230:237], v[74:77], v178, v178 op_sel_hi:[0,0,0]
	v_mfma_scale_f32_16x16x128_f8f6f4 v[78:81], v[190:197], v[230:237], v[78:81], v178, v178 op_sel_hi:[0,0,0]
	v_mfma_scale_f32_16x16x128_f8f6f4 v[70:73], v[198:205], v[230:237], v[70:73], v178, v178 op_sel_hi:[0,0,0]
	ds_read_b128 v[222:225], v2 offset:0x3000
	ds_read_b128 v[226:229], v4 offset:0x3000
	ds_read_b128 v[230:233], v2 offset:0x3800
	ds_read_b128 v[234:237], v4 offset:0x3800
	s_waitcnt lgkmcnt(4)
	v_mfma_scale_f32_16x16x128_f8f6f4 v[66:69], v[158:165], v[206:213], v[66:69], v178, v178 op_sel_hi:[0,0,0]
	v_mfma_scale_f32_16x16x128_f8f6f4 v[58:61], v[182:189], v[206:213], v[58:61], v178, v178 op_sel_hi:[0,0,0]
	v_mfma_scale_f32_16x16x128_f8f6f4 v[62:65], v[190:197], v[206:213], v[62:65], v178, v178 op_sel_hi:[0,0,0]
	v_mfma_scale_f32_16x16x128_f8f6f4 v[54:57], v[198:205], v[206:213], v[54:57], v178, v178 op_sel_hi:[0,0,0]
	v_mfma_scale_f32_16x16x128_f8f6f4 v[50:53], v[158:165], v[214:221], v[50:53], v178, v178 op_sel_hi:[0,0,0]
	v_mfma_scale_f32_16x16x128_f8f6f4 v[42:45], v[182:189], v[214:221], v[42:45], v178, v178 op_sel_hi:[0,0,0]
	v_mfma_scale_f32_16x16x128_f8f6f4 v[46:49], v[190:197], v[214:221], v[46:49], v178, v178 op_sel_hi:[0,0,0]
	v_mfma_scale_f32_16x16x128_f8f6f4 v[38:41], v[198:205], v[214:221], v[38:41], v178, v178 op_sel_hi:[0,0,0]
	s_waitcnt lgkmcnt(0)
	v_mfma_scale_f32_16x16x128_f8f6f4 v[34:37], v[158:165], v[222:229], v[34:37], v178, v178 op_sel_hi:[0,0,0]
	v_mfma_scale_f32_16x16x128_f8f6f4 v[26:29], v[182:189], v[222:229], v[26:29], v178, v178 op_sel_hi:[0,0,0]
	v_mfma_scale_f32_16x16x128_f8f6f4 v[30:33], v[190:197], v[222:229], v[30:33], v178, v178 op_sel_hi:[0,0,0]
	v_mfma_scale_f32_16x16x128_f8f6f4 v[22:25], v[198:205], v[222:229], v[22:25], v178, v178 op_sel_hi:[0,0,0]
	v_mfma_scale_f32_16x16x128_f8f6f4 v[18:21], v[158:165], v[230:237], v[18:21], v178, v178 op_sel_hi:[0,0,0]
	v_mfma_scale_f32_16x16x128_f8f6f4 v[10:13], v[182:189], v[230:237], v[10:13], v178, v178 op_sel_hi:[0,0,0]
	v_mfma_scale_f32_16x16x128_f8f6f4 v[14:17], v[190:197], v[230:237], v[14:17], v178, v178 op_sel_hi:[0,0,0]
	v_mfma_scale_f32_16x16x128_f8f6f4 v[6:9], v[198:205], v[230:237], v[6:9], v178, v178 op_sel_hi:[0,0,0]
	s_branch .LBB0_1032
.Lp5a_ybody:
	s_and_b32 s13, s31, 0x10000
	v_add_u32_e32 v2, s13, v249
	v_xor_b32_e32 v4, 64, v2
	v_or_b32_e32 v5, s13, v250
	v_xor_b32_e32 v166, 64, v5
	ds_read_b128 v[158:161], v5 offset:0
	ds_read_b128 v[162:165], v166 offset:0
	ds_read_b128 v[206:209], v2 offset:0
	ds_read_b128 v[210:213], v4 offset:0
	ds_read_b128 v[182:185], v5 offset:0x800
	ds_read_b128 v[186:189], v166 offset:0x800
	ds_read_b128 v[190:193], v5 offset:0x1000
	ds_read_b128 v[194:197], v166 offset:0x1000
	ds_read_b128 v[198:201], v5 offset:0x1800
	ds_read_b128 v[202:205], v166 offset:0x1800
	ds_read_b128 v[214:217], v2 offset:0x800
	ds_read_b128 v[218:221], v4 offset:0x800
	ds_read_b128 v[222:225], v2 offset:0x1000
	ds_read_b128 v[226:229], v4 offset:0x1000
	ds_read_b128 v[230:233], v2 offset:0x1800
	ds_read_b128 v[234:237], v4 offset:0x1800
	s_nop 0
	s_waitcnt lgkmcnt(12)
	v_mfma_scale_f32_16x16x128_f8f6f4 v[130:133], v[158:165], v[206:213], v[130:133], v178, v178 op_sel_hi:[0,0,0]
	s_waitcnt lgkmcnt(10)
	v_mfma_scale_f32_16x16x128_f8f6f4 v[122:125], v[182:189], v[206:213], v[122:125], v178, v178 op_sel_hi:[0,0,0]
	s_waitcnt lgkmcnt(8)
	v_mfma_scale_f32_16x16x128_f8f6f4 v[126:129], v[190:197], v[206:213], v[126:129], v178, v178 op_sel_hi:[0,0,0]
	s_waitcnt lgkmcnt(6)
	v_mfma_scale_f32_16x16x128_f8f6f4 v[118:121], v[198:205], v[206:213], v[118:121], v178, v178 op_sel_hi:[0,0,0]
	s_waitcnt lgkmcnt(4)
	v_mfma_scale_f32_16x16x128_f8f6f4 v[114:117], v[158:165], v[214:221], v[114:117], v178, v178 op_sel_hi:[0,0,0]
	v_mfma_scale_f32_16x16x128_f8f6f4 v[106:109], v[182:189], v[214:221], v[106:109], v178, v178 op_sel_hi:[0,0,0]
	v_mfma_scale_f32_16x16x128_f8f6f4 v[110:113], v[190:197], v[214:221], v[110:113], v178, v178 op_sel_hi:[0,0,0]
	v_mfma_scale_f32_16x16x128_f8f6f4 v[102:105], v[198:205], v[214:221], v[102:105], v178, v178 op_sel_hi:[0,0,0]
	ds_read_b128 v[206:209], v2 offset:0x2000
	ds_read_b128 v[210:213], v4 offset:0x2000
	ds_read_b128 v[214:217], v2 offset:0x2800
	ds_read_b128 v[218:221], v4 offset:0x2800
	s_waitcnt lgkmcnt(4)
	v_mfma_scale_f32_16x16x128_f8f6f4 v[98:101], v[158:165], v[222:229], v[98:101], v178, v178 op_sel_hi:[0,0,0]
	v_mfma_scale_f32_16x16x128_f8f6f4 v[90:93], v[182:189], v[222:229], v[90:93], v178, v178 op_sel_hi:[0,0,0]
	v_mfma_scale_f32_16x16x128_f8f6f4 v[94:97], v[190:197], v[222:229], v[94:97], v178, v178 op_sel_hi:[0,0,0]
	v_mfma_scale_f32_16x16x128_f8f6f4 v[86:89], v[198:205], v[222:229], v[86:89], v178, v178 op_sel_hi:[0,0,0]
	v_mfma_scale_f32_16x16x128_f8f6f4 v[82:85], v[158:165], v[230:237], v[82:85], v178, v178 op_sel_hi:[0,0,0]
	v_mfma_scale_f32_16x16x128_f8f6f4 v[74:77], v[182:189], v[230:237], v[74:77], v178, v178 op_sel_hi:[0,0,0]
	v_mfma_scale_f32_16x16x128_f8f6f4 v[78:81], v[190:197], v[230:237], v[78:81], v178, v178 op_sel_hi:[0,0,0]
	v_mfma_scale_f32_16x16x128_f8f6f4 v[70:73], v[198:205], v[230:237], v[70:73], v178, v178 op_sel_hi:[0,0,0]
	ds_read_b128 v[222:225], v2 offset:0x3000
	ds_read_b128 v[226:229], v4 offset:0x3000
	ds_read_b128 v[230:233], v2 offset:0x3800
	ds_read_b128 v[234:237], v4 offset:0x3800
	s_waitcnt lgkmcnt(0)
	s_branch .LBB0_1032

.LBB0_1194:
	s_lshl_b32 s30, s30, 15
	v_add_u32_e32 v130, s30, v249
	v_xor_b32_e32 v133, 64, v130
	s_bitset1_b32 s30, 16
	v_or_b32_e32 v135, s30, v251
	v_xor_b32_e32 v137, 64, v135
	ds_read_b128 v[184:187], v135 offset:0
	ds_read_b128 v[188:191], v137 offset:0
	ds_read_b128 v[216:219], v130 offset:0
	ds_read_b128 v[220:223], v133 offset:0
	ds_read_b128 v[192:195], v135 offset:0x800
	ds_read_b128 v[196:199], v137 offset:0x800
	ds_read_b128 v[200:203], v135 offset:0x1000
	ds_read_b128 v[204:207], v137 offset:0x1000
	ds_read_b128 v[208:211], v135 offset:0x1800
	ds_read_b128 v[212:215], v137 offset:0x1800
	ds_read_b128 v[224:227], v130 offset:0x800
	ds_read_b128 v[228:231], v133 offset:0x800
	ds_read_b128 v[232:235], v130 offset:0x1000
	ds_read_b128 v[236:239], v133 offset:0x1000
	ds_read_b128 v[240:243], v130 offset:0x1800
	ds_read_b128 v[244:247], v133 offset:0x1800
	s_nop 0
	s_waitcnt lgkmcnt(12)
	v_mfma_scale_f32_16x16x128_f8f6f4 v[126:129], v[184:191], v[216:223], v[126:129], v179, v179 op_sel_hi:[0,0,0]
	s_waitcnt lgkmcnt(10)
	v_mfma_scale_f32_16x16x128_f8f6f4 v[122:125], v[192:199], v[216:223], v[122:125], v179, v179 op_sel_hi:[0,0,0]
	s_waitcnt lgkmcnt(8)
	v_mfma_scale_f32_16x16x128_f8f6f4 v[118:121], v[200:207], v[216:223], v[118:121], v179, v179 op_sel_hi:[0,0,0]
	s_waitcnt lgkmcnt(6)
	v_mfma_scale_f32_16x16x128_f8f6f4 v[114:117], v[208:215], v[216:223], v[114:117], v179, v179 op_sel_hi:[0,0,0]
	s_waitcnt lgkmcnt(4)
	v_mfma_scale_f32_16x16x128_f8f6f4 v[110:113], v[184:191], v[224:231], v[110:113], v179, v179 op_sel_hi:[0,0,0]
	v_mfma_scale_f32_16x16x128_f8f6f4 v[106:109], v[192:199], v[224:231], v[106:109], v179, v179 op_sel_hi:[0,0,0]
	v_mfma_scale_f32_16x16x128_f8f6f4 v[102:105], v[200:207], v[224:231], v[102:105], v179, v179 op_sel_hi:[0,0,0]
	v_mfma_scale_f32_16x16x128_f8f6f4 v[98:101], v[208:215], v[224:231], v[98:101], v179, v179 op_sel_hi:[0,0,0]
	ds_read_b128 v[216:219], v130 offset:0x2000
	ds_read_b128 v[220:223], v133 offset:0x2000
	ds_read_b128 v[224:227], v130 offset:0x2800
	ds_read_b128 v[228:231], v133 offset:0x2800
	s_waitcnt lgkmcnt(4)
	v_mfma_scale_f32_16x16x128_f8f6f4 v[94:97], v[184:191], v[232:239], v[94:97], v179, v179 op_sel_hi:[0,0,0]
	v_mfma_scale_f32_16x16x128_f8f6f4 v[90:93], v[192:199], v[232:239], v[90:93], v179, v179 op_sel_hi:[0,0,0]
	v_mfma_scale_f32_16x16x128_f8f6f4 v[86:89], v[200:207], v[232:239], v[86:89], v179, v179 op_sel_hi:[0,0,0]
	v_mfma_scale_f32_16x16x128_f8f6f4 v[82:85], v[208:215], v[232:239], v[82:85], v179, v179 op_sel_hi:[0,0,0]
	v_mfma_scale_f32_16x16x128_f8f6f4 v[78:81], v[184:191], v[240:247], v[78:81], v179, v179 op_sel_hi:[0,0,0]
	v_mfma_scale_f32_16x16x128_f8f6f4 v[74:77], v[192:199], v[240:247], v[74:77], v179, v179 op_sel_hi:[0,0,0]
	v_mfma_scale_f32_16x16x128_f8f6f4 v[70:73], v[200:207], v[240:247], v[70:73], v179, v179 op_sel_hi:[0,0,0]
	v_mfma_scale_f32_16x16x128_f8f6f4 v[66:69], v[208:215], v[240:247], v[66:69], v179, v179 op_sel_hi:[0,0,0]
	ds_read_b128 v[232:235], v130 offset:0x3000
	ds_read_b128 v[236:239], v133 offset:0x3000
	ds_read_b128 v[240:243], v130 offset:0x3800
	ds_read_b128 v[244:247], v133 offset:0x3800
	s_waitcnt lgkmcnt(4)
	v_mfma_scale_f32_16x16x128_f8f6f4 v[62:65], v[184:191], v[216:223], v[62:65], v179, v179 op_sel_hi:[0,0,0]
	v_mfma_scale_f32_16x16x128_f8f6f4 v[58:61], v[192:199], v[216:223], v[58:61], v179, v179 op_sel_hi:[0,0,0]
	v_mfma_scale_f32_16x16x128_f8f6f4 v[54:57], v[200:207], v[216:223], v[54:57], v179, v179 op_sel_hi:[0,0,0]
	v_mfma_scale_f32_16x16x128_f8f6f4 v[50:53], v[208:215], v[216:223], v[50:53], v179, v179 op_sel_hi:[0,0,0]
	v_mfma_scale_f32_16x16x128_f8f6f4 v[46:49], v[184:191], v[224:231], v[46:49], v179, v179 op_sel_hi:[0,0,0]
	v_mfma_scale_f32_16x16x128_f8f6f4 v[42:45], v[192:199], v[224:231], v[42:45], v179, v179 op_sel_hi:[0,0,0]
	v_mfma_scale_f32_16x16x128_f8f6f4 v[38:41], v[200:207], v[224:231], v[38:41], v179, v179 op_sel_hi:[0,0,0]
	v_mfma_scale_f32_16x16x128_f8f6f4 v[34:37], v[208:215], v[224:231], v[34:37], v179, v179 op_sel_hi:[0,0,0]
	s_waitcnt lgkmcnt(0)
	v_mfma_scale_f32_16x16x128_f8f6f4 v[30:33], v[184:191], v[232:239], v[30:33], v179, v179 op_sel_hi:[0,0,0]
	v_mfma_scale_f32_16x16x128_f8f6f4 v[26:29], v[192:199], v[232:239], v[26:29], v179, v179 op_sel_hi:[0,0,0]
	v_mfma_scale_f32_16x16x128_f8f6f4 v[22:25], v[200:207], v[232:239], v[22:25], v179, v179 op_sel_hi:[0,0,0]
	v_mfma_scale_f32_16x16x128_f8f6f4 v[18:21], v[208:215], v[232:239], v[18:21], v179, v179 op_sel_hi:[0,0,0]
	v_mfma_scale_f32_16x16x128_f8f6f4 v[14:17], v[184:191], v[240:247], v[14:17], v179, v179 op_sel_hi:[0,0,0]
	v_mfma_scale_f32_16x16x128_f8f6f4 v[10:13], v[192:199], v[240:247], v[10:13], v179, v179 op_sel_hi:[0,0,0]
	v_mfma_scale_f32_16x16x128_f8f6f4 v[6:9], v[200:207], v[240:247], v[6:9], v179, v179 op_sel_hi:[0,0,0]
	v_mfma_scale_f32_16x16x128_f8f6f4 v[2:5], v[208:215], v[240:247], v[2:5], v179, v179 op_sel_hi:[0,0,0]
	s_andn2_b64 vcc, exec, s[58:59]
	s_cbranch_vccnz .LBB0_1182

.LBB0_1233:
	s_and_b32 s20, s31, 0x10000
	v_or_b32_e32 v5, s20, v250
	v_add_u32_e32 v2, s20, v249
	v_xor_b32_e32 v4, 64, v2
	v_xor_b32_e32 v182, 64, v5
	ds_read_b128 v[154:157], v5 offset:0
	ds_read_b128 v[158:161], v182 offset:0
	ds_read_b128 v[186:189], v2 offset:0
	ds_read_b128 v[190:193], v4 offset:0
	ds_read_b128 v[162:165], v5 offset:0x800
	ds_read_b128 v[166:169], v182 offset:0x800
	ds_read_b128 v[170:173], v5 offset:0x1000
	ds_read_b128 v[174:177], v182 offset:0x1000
	ds_read_b128 v[178:181], v5 offset:0x1800
	ds_read_b128 v[182:185], v182 offset:0x1800
	ds_read_b128 v[194:197], v2 offset:0x800
	ds_read_b128 v[198:201], v4 offset:0x800
	ds_read_b128 v[202:205], v2 offset:0x1000
	ds_read_b128 v[206:209], v4 offset:0x1000
	ds_read_b128 v[210:213], v2 offset:0x1800
	ds_read_b128 v[214:217], v4 offset:0x1800
	s_nop 0
	s_waitcnt lgkmcnt(12)
	v_mfma_scale_f32_16x16x128_f8f6f4 v[130:133], v[154:161], v[186:193], v[130:133], v153, v153 op_sel_hi:[0,0,0]
	s_waitcnt lgkmcnt(10)
	v_mfma_scale_f32_16x16x128_f8f6f4 v[126:129], v[162:169], v[186:193], v[126:129], v153, v153 op_sel_hi:[0,0,0]
	s_waitcnt lgkmcnt(8)
	v_mfma_scale_f32_16x16x128_f8f6f4 v[122:125], v[170:177], v[186:193], v[122:125], v153, v153 op_sel_hi:[0,0,0]
	s_waitcnt lgkmcnt(6)
	v_mfma_scale_f32_16x16x128_f8f6f4 v[118:121], v[178:185], v[186:193], v[118:121], v153, v153 op_sel_hi:[0,0,0]
	s_waitcnt lgkmcnt(4)
	v_mfma_scale_f32_16x16x128_f8f6f4 v[114:117], v[154:161], v[194:201], v[114:117], v153, v153 op_sel_hi:[0,0,0]
	v_mfma_scale_f32_16x16x128_f8f6f4 v[110:113], v[162:169], v[194:201], v[110:113], v153, v153 op_sel_hi:[0,0,0]
	v_mfma_scale_f32_16x16x128_f8f6f4 v[106:109], v[170:177], v[194:201], v[106:109], v153, v153 op_sel_hi:[0,0,0]
	v_mfma_scale_f32_16x16x128_f8f6f4 v[102:105], v[178:185], v[194:201], v[102:105], v153, v153 op_sel_hi:[0,0,0]
	ds_read_b128 v[186:189], v2 offset:0x2000
	ds_read_b128 v[190:193], v4 offset:0x2000
	ds_read_b128 v[194:197], v2 offset:0x2800
	ds_read_b128 v[198:201], v4 offset:0x2800
	s_waitcnt lgkmcnt(4)
	v_mfma_scale_f32_16x16x128_f8f6f4 v[98:101], v[154:161], v[202:209], v[98:101], v153, v153 op_sel_hi:[0,0,0]
	v_mfma_scale_f32_16x16x128_f8f6f4 v[94:97], v[162:169], v[202:209], v[94:97], v153, v153 op_sel_hi:[0,0,0]
	v_mfma_scale_f32_16x16x128_f8f6f4 v[90:93], v[170:177], v[202:209], v[90:93], v153, v153 op_sel_hi:[0,0,0]
	v_mfma_scale_f32_16x16x128_f8f6f4 v[86:89], v[178:185], v[202:209], v[86:89], v153, v153 op_sel_hi:[0,0,0]
	v_mfma_scale_f32_16x16x128_f8f6f4 v[82:85], v[154:161], v[210:217], v[82:85], v153, v153 op_sel_hi:[0,0,0]
	v_mfma_scale_f32_16x16x128_f8f6f4 v[78:81], v[162:169], v[210:217], v[78:81], v153, v153 op_sel_hi:[0,0,0]
	v_mfma_scale_f32_16x16x128_f8f6f4 v[74:77], v[170:177], v[210:217], v[74:77], v153, v153 op_sel_hi:[0,0,0]
	v_mfma_scale_f32_16x16x128_f8f6f4 v[70:73], v[178:185], v[210:217], v[70:73], v153, v153 op_sel_hi:[0,0,0]
	ds_read_b128 v[202:205], v2 offset:0x3000
	ds_read_b128 v[206:209], v4 offset:0x3000
	ds_read_b128 v[210:213], v2 offset:0x3800
	ds_read_b128 v[214:217], v4 offset:0x3800
	s_waitcnt lgkmcnt(4)
	v_mfma_scale_f32_16x16x128_f8f6f4 v[66:69], v[154:161], v[186:193], v[66:69], v153, v153 op_sel_hi:[0,0,0]
	v_mfma_scale_f32_16x16x128_f8f6f4 v[62:65], v[162:169], v[186:193], v[62:65], v153, v153 op_sel_hi:[0,0,0]
	v_mfma_scale_f32_16x16x128_f8f6f4 v[58:61], v[170:177], v[186:193], v[58:61], v153, v153 op_sel_hi:[0,0,0]
	v_mfma_scale_f32_16x16x128_f8f6f4 v[54:57], v[178:185], v[186:193], v[54:57], v153, v153 op_sel_hi:[0,0,0]
	v_mfma_scale_f32_16x16x128_f8f6f4 v[50:53], v[154:161], v[194:201], v[50:53], v153, v153 op_sel_hi:[0,0,0]
	v_mfma_scale_f32_16x16x128_f8f6f4 v[46:49], v[162:169], v[194:201], v[46:49], v153, v153 op_sel_hi:[0,0,0]
	v_mfma_scale_f32_16x16x128_f8f6f4 v[42:45], v[170:177], v[194:201], v[42:45], v153, v153 op_sel_hi:[0,0,0]
	v_mfma_scale_f32_16x16x128_f8f6f4 v[38:41], v[178:185], v[194:201], v[38:41], v153, v153 op_sel_hi:[0,0,0]
	s_waitcnt lgkmcnt(0)
	v_mfma_scale_f32_16x16x128_f8f6f4 v[34:37], v[154:161], v[202:209], v[34:37], v153, v153 op_sel_hi:[0,0,0]
	v_mfma_scale_f32_16x16x128_f8f6f4 v[30:33], v[162:169], v[202:209], v[30:33], v153, v153 op_sel_hi:[0,0,0]
	v_mfma_scale_f32_16x16x128_f8f6f4 v[26:29], v[170:177], v[202:209], v[26:29], v153, v153 op_sel_hi:[0,0,0]
	v_mfma_scale_f32_16x16x128_f8f6f4 v[22:25], v[178:185], v[202:209], v[22:25], v153, v153 op_sel_hi:[0,0,0]
	v_mfma_scale_f32_16x16x128_f8f6f4 v[18:21], v[154:161], v[210:217], v[18:21], v153, v153 op_sel_hi:[0,0,0]
	v_mfma_scale_f32_16x16x128_f8f6f4 v[14:17], v[162:169], v[210:217], v[14:17], v153, v153 op_sel_hi:[0,0,0]
	v_mfma_scale_f32_16x16x128_f8f6f4 v[10:13], v[170:177], v[210:217], v[10:13], v153, v153 op_sel_hi:[0,0,0]
	v_mfma_scale_f32_16x16x128_f8f6f4 v[6:9], v[178:185], v[210:217], v[6:9], v153, v153 op_sel_hi:[0,0,0]
	s_branch .LBB0_1219
